# speedup vs baseline: 1.0365x; 1.0082x over previous
_Z10scan_pass1PKDF16_S0_PKfS0_S2_S2_PDF16_PfS4_S2_S3_:
	s_load_dwordx16 s[8:23], s[0:1], 0x0
	s_load_dwordx4 s[24:27], s[0:1], 0x40
	s_load_dwordx2 s[28:29], s[0:1], 0x50
	s_mov_b32 s64, 0x3d800000
	s_mov_b32 s65, 0x3fb8aa3b
	s_mov_b32 s66, 0x3f317218
	s_mov_b32 s84, 0x40800000
	s_mov_b32 s86, 0x41800000
	s_lshl_b32 s5, s4, 11
	s_lshl_b32 s6, s3, 5
	s_add_i32 s5, s5, s6
	s_lshl_b32 s6, s4, 6
	s_add_i32 s6, s6, s3
	s_getreg_b32 s7, hwreg(HW_REG_HW_ID, 0, 6)
	s_and_b32 s69, s7, 3
	s_lshl_b32 s69, s69, 2
	s_lshr_b32 s7, s7, 4
	s_or_b32 s7, s7, s69
	s_cmp_eq_u32 s7, 0
	s_cbranch_scc1 .Lstag_p1_done
.Lstag_p1_loop:
	s_sleep 14
	s_sub_u32 s7, s7, 1
	s_cmp_lg_u32 s7, 0
	s_cbranch_scc1 .Lstag_p1_loop

_Z10scan_pass2PKDF16_PKfS2_S0_S2_S0_PDF16_S2_:
	s_load_dwordx16 s[8:23], s[0:1], 0x0
	s_mov_b32 s28, 0x3e800000
	s_mov_b32 s29, 0x3c800000
	s_mov_b32 s30, 0x40800000
	s_lshl_b32 s5, s4, 11
	s_lshl_b32 s6, s3, 5
	s_add_i32 s5, s5, s6
	s_lshl_b32 s6, s4, 6
	s_add_i32 s6, s6, s3
	s_getreg_b32 s7, hwreg(HW_REG_HW_ID, 0, 6)
	s_and_b32 s31, s7, 3
	s_lshl_b32 s31, s31, 2
	s_lshr_b32 s7, s7, 4
	s_or_b32 s7, s7, s31
	s_cmp_eq_u32 s7, 0
	s_cbranch_scc1 .Lstag_p2_done
